# fp8 GEMM (moe1, glu): LDS operand reads bank-conflict-free by swapping the two 16-byte halves of each 32-byte K slice for odd k-groups (same products, f32 accumulate)
# speedup vs baseline: 1.0074x; 1.0073x over previous
.LBB0_495:
	s_add_u32 s46, s4, 0x910100
	s_addc_u32 s47, s5, 0
	s_mul_i32 s24, s88, 0x66000
	s_mul_hi_i32 s1, s88, 0x66000
	s_add_u32 s24, s4, s24
	v_readfirstlane_b32 s30, v5
	s_addc_u32 s1, s5, s1
	s_mul_i32 s21, s21, s30
	s_add_u32 s60, s24, 0x12000
	s_mul_hi_u32 s21, s30, s21
	s_addc_u32 s61, s1, 0
	s_abs_i32 s24, s8
	s_add_i32 s30, s30, s21
	s_mul_hi_u32 s21, s24, s30
	s_mul_i32 s30, s21, s7
	s_sub_i32 s24, s24, s30
	s_ashr_i32 s1, s8, 31
	s_add_i32 s30, s21, 1
	s_sub_i32 s31, s24, s7
	s_cmp_ge_u32 s24, s7
	s_cselect_b32 s21, s30, s21
	s_cselect_b32 s24, s31, s24
	s_add_i32 s30, s21, 1
	s_cmp_ge_u32 s24, s7
	s_cselect_b32 s7, s30, s21
	s_xor_b32 s7, s7, s1
	s_sub_i32 s62, s7, s1
	s_lshl_b32 s7, s23, 5
	s_and_b32 s64, s7, 0x60
	s_lshl_b32 s63, s22, 6
	s_lshl_b32 s1, s22, 13
	s_lshl_b32 s7, s64, 7
	s_add_i32 s65, s15, 0x18400
	s_add_i32 s66, s15, 0x1a400
	v_lshl_add_u64 v[0:1], v[0:1], 0, s[26:27]
	s_mov_b32 m0, s65
	s_add_u32 s48, s4, 0x12910180
	s_waitcnt vmcnt(2)
	s_barrier
	global_load_lds_dwordx4 v[0:1], off
	v_lshl_add_u64 v[0:1], v[2:3], 0, s[26:27]
	s_mov_b32 m0, s66
	s_addc_u32 s49, s5, 0
	s_add_i32 s67, s15, 0x8400
	s_add_i32 s68, s15, 0xa400
	v_mov_b32_e32 v199, v113
	global_load_lds_dwordx4 v[0:1], off
	v_lshl_add_u64 v[0:1], s[48:49], 0, v[112:113]
	s_mov_b32 m0, s67
	s_add_u32 s4, s2, 0x20080
	global_load_lds_dwordx4 v[0:1], off
	v_lshl_add_u64 v[0:1], s[48:49], 0, v[198:199]
	s_mov_b32 m0, s68
	s_addc_u32 s5, s3, 0
	s_add_i32 s69, s15, 0x1c400
	global_load_lds_dwordx4 v[0:1], off
	v_lshl_add_u64 v[0:1], s[4:5], 0, v[196:197]
	s_mov_b32 m0, s69
	s_add_i32 s70, s15, 0x1e400
	global_load_lds_dwordx4 v[0:1], off
	v_lshl_add_u64 v[0:1], s[4:5], 0, v[194:195]
	s_mov_b32 m0, s70
	v_lshlrev_b32_e32 v2, 6, v4
	global_load_lds_dwordx4 v[0:1], off
	v_lshlrev_b32_e32 v0, 1, v4
	v_lshlrev_b32_e32 v3, 2, v4
	v_and_b32_e32 v0, 32, v0
	v_lshlrev_b32_e32 v1, 5, v4
	v_and_b32_e32 v2, 0x3c0, v2
	v_and_b32_e32 v3, 32, v3
	v_and_b32_e32 v1, 0x400, v1
	v_bitop3_b32 v0, v2, v3, v0 bitop3:0x36
	s_waitcnt vmcnt(6)
	s_add_i32 s4, s7, 0
	s_add_i32 s1, s1, 0
	v_add3_u32 v2, s4, v0, v1
	v_add_u32_e32 v0, s1, v0
	s_cmpk_lt_u32 s6, 0x100
	s_mov_b32 s71, 0
	v_add_u32_e32 v226, 0x10400, v2
	v_add_u32_e32 v227, 0x14400, v2
	v_add_u32_e32 v228, 0x18400, v2
	v_add_u32_e32 v229, 0x1c400, v2
	s_cselect_b64 s[50:51], -1, 0
	v_add_u32_e32 v230, 0x10410, v2
	v_add_u32_e32 v231, 0x10c00, v2
	v_add_u32_e32 v232, 0x10c10, v2
	v_add_u32_e32 v233, 0x14410, v2
	v_add_u32_e32 v234, 0x14c00, v2
	v_add_u32_e32 v235, 0x14c10, v2
	v_add_u32_e32 v236, 0x18410, v2
	v_add_u32_e32 v237, 0x18c00, v2
	v_add_u32_e32 v238, 0x18c10, v2
	v_add_u32_e32 v239, 0x1c410, v2
	v_add_u32_e32 v240, 0x1cc00, v2
	v_add_u32_e32 v241, 0x1cc10, v2
	s_lshl_b32 s72, s64, 2
	v_add_u32_e32 v242, v0, v1
	v_mbcnt_lo_u32_b32 v221, -1, 0
	v_mbcnt_hi_u32_b32 v221, -1, v221
	v_and_b32_e32 v221, 16, v221
	v_add_u32_e32 v226, v226, v221
	v_add_u32_e32 v227, v227, v221
	v_add_u32_e32 v228, v228, v221
	v_add_u32_e32 v229, v229, v221
	v_add_u32_e32 v231, v231, v221
	v_add_u32_e32 v234, v234, v221
	v_add_u32_e32 v237, v237, v221
	v_add_u32_e32 v240, v240, v221
	v_sub_u32_e32 v230, v230, v221
	v_sub_u32_e32 v232, v232, v221
	v_sub_u32_e32 v233, v233, v221
	v_sub_u32_e32 v235, v235, v221
	v_sub_u32_e32 v236, v236, v221
	v_sub_u32_e32 v238, v238, v221
	v_sub_u32_e32 v239, v239, v221
	v_sub_u32_e32 v241, v241, v221
	v_sub_u32_e32 v245, v242, v221
	v_add_u32_e32 v242, v242, v221
	s_barrier
	s_branch .LBB0_498

.LBB0_502:
	s_waitcnt vmcnt(8)
	s_add_u32 s6, s2, 0x80
	s_waitcnt lgkmcnt(0)
	s_addc_u32 s7, s3, 0
	s_and_b64 s[4:5], s[4:5], exec
	s_cselect_b32 s7, s43, s7
	s_cselect_b32 s6, s42, s6
	s_cselect_b32 s5, s1, s23
	s_cselect_b32 s4, s21, s22
	s_barrier
	s_setprio 1
	s_waitcnt lgkmcnt(0)
	v_mfma_scale_f32_16x16x128_f8f6f4 v[190:193], v[24:31], v[56:63], v[190:193], v216, v216 op_sel_hi:[0,0,0]
	v_mfma_scale_f32_16x16x128_f8f6f4 v[178:181], v[16:23], v[56:63], v[178:181], v216, v216 op_sel_hi:[0,0,0]
	v_mfma_scale_f32_16x16x128_f8f6f4 v[174:177], v[24:31], v[48:55], v[174:177], v216, v216 op_sel_hi:[0,0,0]
	v_mfma_scale_f32_16x16x128_f8f6f4 v[162:165], v[16:23], v[48:55], v[162:165], v216, v216 op_sel_hi:[0,0,0]
	v_mfma_scale_f32_16x16x128_f8f6f4 v[158:161], v[24:31], v[40:47], v[158:161], v216, v216 op_sel_hi:[0,0,0]
	v_mfma_scale_f32_16x16x128_f8f6f4 v[146:149], v[16:23], v[40:47], v[146:149], v216, v216 op_sel_hi:[0,0,0]
	v_mfma_scale_f32_16x16x128_f8f6f4 v[142:145], v[24:31], v[32:39], v[142:145], v216, v216 op_sel_hi:[0,0,0]
	v_mfma_scale_f32_16x16x128_f8f6f4 v[130:133], v[16:23], v[32:39], v[130:133], v216, v216 op_sel_hi:[0,0,0]
	s_setprio 0
	s_setprio 1
	v_mfma_scale_f32_16x16x128_f8f6f4 v[186:189], v[0:7], v[56:63], v[186:189], v216, v216 op_sel_hi:[0,0,0]
	v_mfma_scale_f32_16x16x128_f8f6f4 v[182:185], v[8:15], v[56:63], v[182:185], v216, v216 op_sel_hi:[0,0,0]
	v_mfma_scale_f32_16x16x128_f8f6f4 v[170:173], v[0:7], v[48:55], v[170:173], v216, v216 op_sel_hi:[0,0,0]
	v_mfma_scale_f32_16x16x128_f8f6f4 v[166:169], v[8:15], v[48:55], v[166:169], v216, v216 op_sel_hi:[0,0,0]
	v_mfma_scale_f32_16x16x128_f8f6f4 v[154:157], v[0:7], v[40:47], v[154:157], v216, v216 op_sel_hi:[0,0,0]
	v_mfma_scale_f32_16x16x128_f8f6f4 v[150:153], v[8:15], v[40:47], v[150:153], v216, v216 op_sel_hi:[0,0,0]
	v_mfma_scale_f32_16x16x128_f8f6f4 v[138:141], v[0:7], v[32:39], v[138:141], v216, v216 op_sel_hi:[0,0,0]
	v_mfma_scale_f32_16x16x128_f8f6f4 v[134:137], v[8:15], v[32:39], v[134:137], v216, v216 op_sel_hi:[0,0,0]
	s_setprio 0
	s_barrier
	s_mov_b32 m0, s16
	v_lshl_add_u64 v[246:247], s[4:5], 0, v[196:197]
	s_add_u32 s30, s4, 0x20000
	ds_read_b128 v[32:35], v242 offset:17408
	ds_read_b128 v[36:39], v245 offset:17424
	ds_read_b128 v[40:43], v242 offset:19456
	ds_read_b128 v[44:47], v245 offset:19472
	ds_read_b128 v[48:51], v242 offset:21504
	ds_read_b128 v[52:55], v245 offset:21520
	ds_read_b128 v[56:59], v242 offset:23552
	ds_read_b128 v[60:63], v245 offset:23568
	global_load_lds_dwordx4 v[246:247], off
	v_lshl_add_u64 v[248:249], s[4:5], 0, v[194:195]
	s_mov_b32 m0, s17
	s_addc_u32 s31, s5, 0
	global_load_lds_dwordx4 v[248:249], off
	v_lshl_add_u64 v[250:251], s[30:31], 0, v[196:197]
	s_mov_b32 m0, s18
	v_mov_b32_e32 v199, v113
	global_load_lds_dwordx4 v[250:251], off
	v_lshl_add_u64 v[250:251], s[30:31], 0, v[194:195]
	s_mov_b32 m0, s19
	v_lshl_add_u64 v[252:253], s[6:7], 0, v[198:199]
	global_load_lds_dwordx4 v[250:251], off
	s_mov_b32 m0, s28
	v_lshl_add_u64 v[250:251], s[6:7], 0, v[112:113]
	global_load_lds_dwordx4 v112, s[6:7]
	s_mov_b32 m0, s29
	s_nop 0
	global_load_lds_dwordx4 v198, s[6:7]
	s_waitcnt vmcnt(8)
	s_waitcnt lgkmcnt(0)
	s_barrier
	s_setprio 1
	s_waitcnt lgkmcnt(0)
	v_mfma_scale_f32_16x16x128_f8f6f4 v[126:129], v[24:31], v[32:39], v[126:129], v216, v216 op_sel_hi:[0,0,0]
	v_mfma_scale_f32_16x16x128_f8f6f4 v[114:117], v[16:23], v[32:39], v[114:117], v216, v216 op_sel_hi:[0,0,0]
	v_mfma_scale_f32_16x16x128_f8f6f4 v[108:111], v[24:31], v[40:47], v[108:111], v216, v216 op_sel_hi:[0,0,0]
	v_mfma_scale_f32_16x16x128_f8f6f4 v[96:99], v[16:23], v[40:47], v[96:99], v216, v216 op_sel_hi:[0,0,0]
	v_mfma_scale_f32_16x16x128_f8f6f4 v[92:95], v[24:31], v[48:55], v[92:95], v216, v216 op_sel_hi:[0,0,0]
	v_mfma_scale_f32_16x16x128_f8f6f4 v[80:83], v[16:23], v[48:55], v[80:83], v216, v216 op_sel_hi:[0,0,0]
	v_mfma_scale_f32_16x16x128_f8f6f4 v[76:79], v[24:31], v[56:63], v[76:79], v216, v216 op_sel_hi:[0,0,0]
	v_mfma_scale_f32_16x16x128_f8f6f4 v[68:71], v[16:23], v[56:63], v[68:71], v216, v216 op_sel_hi:[0,0,0]
	s_setprio 0
	s_setprio 1
	v_mfma_scale_f32_16x16x128_f8f6f4 v[122:125], v[0:7], v[32:39], v[122:125], v216, v216 op_sel_hi:[0,0,0]
	v_mfma_scale_f32_16x16x128_f8f6f4 v[118:121], v[8:15], v[32:39], v[118:121], v216, v216 op_sel_hi:[0,0,0]
	v_mfma_scale_f32_16x16x128_f8f6f4 v[104:107], v[0:7], v[40:47], v[104:107], v216, v216 op_sel_hi:[0,0,0]
	v_mfma_scale_f32_16x16x128_f8f6f4 v[100:103], v[8:15], v[40:47], v[100:103], v216, v216 op_sel_hi:[0,0,0]
	v_mfma_scale_f32_16x16x128_f8f6f4 v[88:91], v[0:7], v[48:55], v[88:91], v216, v216 op_sel_hi:[0,0,0]
	v_mfma_scale_f32_16x16x128_f8f6f4 v[84:87], v[8:15], v[48:55], v[84:87], v216, v216 op_sel_hi:[0,0,0]
	v_mfma_scale_f32_16x16x128_f8f6f4 v[72:75], v[0:7], v[56:63], v[72:75], v216, v216 op_sel_hi:[0,0,0]
	v_mfma_scale_f32_16x16x128_f8f6f4 v[64:67], v[8:15], v[56:63], v[64:67], v216, v216 op_sel_hi:[0,0,0]
	s_setprio 0
	s_barrier
	ds_read_b128 v[4:7], v236
	ds_read_b128 v[8:11], v237
	ds_read_b128 v[0:3], v228
	ds_read_b128 v[16:19], v229
	ds_read_b128 v[12:15], v238
	ds_read_b128 v[20:23], v239
	ds_read_b128 v[24:27], v240
	ds_read_b128 v[28:31], v241
	s_mov_b32 m0, s58
	v_lshl_add_u64 v[210:211], s[6:7], 0, v[210:211]
	ds_read_b128 v[32:35], v242 offset:33792
	ds_read_b128 v[36:39], v245 offset:33808
	ds_read_b128 v[40:43], v242 offset:35840
	ds_read_b128 v[44:47], v245 offset:35856
	ds_read_b128 v[48:51], v242 offset:37888
	ds_read_b128 v[52:55], v245 offset:37904
	ds_read_b128 v[56:59], v242 offset:39936
	ds_read_b128 v[60:63], v245 offset:39952
	global_load_lds_dwordx4 v[210:211], off
	v_lshl_add_u64 v[208:209], s[6:7], 0, v[208:209]
	s_mov_b32 m0, s59
	s_nop 0
	global_load_lds_dwordx4 v[208:209], off
	s_waitcnt vmcnt(8)
	s_waitcnt lgkmcnt(0)
	s_barrier
	s_setprio 1
	s_waitcnt lgkmcnt(0)
	v_mfma_scale_f32_16x16x128_f8f6f4 v[190:193], v[0:7], v[32:39], v[190:193], v216, v216 op_sel_hi:[0,0,0]
	v_mfma_scale_f32_16x16x128_f8f6f4 v[178:181], v[8:15], v[32:39], v[178:181], v216, v216 op_sel_hi:[0,0,0]
	v_mfma_scale_f32_16x16x128_f8f6f4 v[174:177], v[0:7], v[40:47], v[174:177], v216, v216 op_sel_hi:[0,0,0]
	v_mfma_scale_f32_16x16x128_f8f6f4 v[162:165], v[8:15], v[40:47], v[162:165], v216, v216 op_sel_hi:[0,0,0]
	v_mfma_scale_f32_16x16x128_f8f6f4 v[158:161], v[0:7], v[48:55], v[158:161], v216, v216 op_sel_hi:[0,0,0]
	v_mfma_scale_f32_16x16x128_f8f6f4 v[146:149], v[8:15], v[48:55], v[146:149], v216, v216 op_sel_hi:[0,0,0]
	v_mfma_scale_f32_16x16x128_f8f6f4 v[142:145], v[0:7], v[56:63], v[142:145], v216, v216 op_sel_hi:[0,0,0]
	v_mfma_scale_f32_16x16x128_f8f6f4 v[130:133], v[8:15], v[56:63], v[130:133], v216, v216 op_sel_hi:[0,0,0]
	s_setprio 0
	s_setprio 1
	v_mfma_scale_f32_16x16x128_f8f6f4 v[186:189], v[16:23], v[32:39], v[186:189], v216, v216 op_sel_hi:[0,0,0]
	v_mfma_scale_f32_16x16x128_f8f6f4 v[182:185], v[24:31], v[32:39], v[182:185], v216, v216 op_sel_hi:[0,0,0]
	v_mfma_scale_f32_16x16x128_f8f6f4 v[170:173], v[16:23], v[40:47], v[170:173], v216, v216 op_sel_hi:[0,0,0]
	v_mfma_scale_f32_16x16x128_f8f6f4 v[166:169], v[24:31], v[40:47], v[166:169], v216, v216 op_sel_hi:[0,0,0]
	v_mfma_scale_f32_16x16x128_f8f6f4 v[154:157], v[16:23], v[48:55], v[154:157], v216, v216 op_sel_hi:[0,0,0]
	v_mfma_scale_f32_16x16x128_f8f6f4 v[150:153], v[24:31], v[48:55], v[150:153], v216, v216 op_sel_hi:[0,0,0]
	v_mfma_scale_f32_16x16x128_f8f6f4 v[138:141], v[16:23], v[56:63], v[138:141], v216, v216 op_sel_hi:[0,0,0]
	v_mfma_scale_f32_16x16x128_f8f6f4 v[134:137], v[24:31], v[56:63], v[134:137], v216, v216 op_sel_hi:[0,0,0]
	s_setprio 0
	s_barrier
	s_mov_b32 m0, s65
	v_lshl_add_u64 v[208:209], v[246:247], 0, s[26:27]
	s_add_u32 s4, s4, 0x20080
	ds_read_b128 v[32:35], v242 offset:50176
	ds_read_b128 v[36:39], v245 offset:50192
	ds_read_b128 v[40:43], v242 offset:52224
	ds_read_b128 v[44:47], v245 offset:52240
	ds_read_b128 v[48:51], v242 offset:54272
	ds_read_b128 v[52:55], v245 offset:54288
	ds_read_b128 v[56:59], v242 offset:56320
	ds_read_b128 v[60:63], v245 offset:56336
	global_load_lds_dwordx4 v[208:209], off
	v_lshl_add_u64 v[208:209], v[248:249], 0, s[26:27]
	s_mov_b32 m0, s66
	s_addc_u32 s5, s5, 0
	global_load_lds_dwordx4 v[208:209], off
	v_lshl_add_u64 v[208:209], s[4:5], 0, v[196:197]
	s_mov_b32 m0, s69
	s_nop 0
	global_load_lds_dwordx4 v[208:209], off
	v_lshl_add_u64 v[208:209], s[4:5], 0, v[194:195]
	s_mov_b32 m0, s70
	s_nop 0
	global_load_lds_dwordx4 v[208:209], off
	v_lshl_add_u64 v[208:209], v[250:251], 0, s[26:27]
	s_mov_b32 m0, s67
	s_nop 0
	global_load_lds_dwordx4 v[208:209], off
	v_lshl_add_u64 v[208:209], v[252:253], 0, s[26:27]
	s_mov_b32 m0, s68
	s_nop 0
	global_load_lds_dwordx4 v[208:209], off
	s_waitcnt vmcnt(8)
	s_waitcnt lgkmcnt(0)
	s_barrier
	s_setprio 1
	s_waitcnt lgkmcnt(0)
	v_mfma_scale_f32_16x16x128_f8f6f4 v[126:129], v[0:7], v[32:39], v[126:129], v216, v216 op_sel_hi:[0,0,0]
	v_mfma_scale_f32_16x16x128_f8f6f4 v[114:117], v[8:15], v[32:39], v[114:117], v216, v216 op_sel_hi:[0,0,0]
	v_mfma_scale_f32_16x16x128_f8f6f4 v[108:111], v[0:7], v[40:47], v[108:111], v216, v216 op_sel_hi:[0,0,0]
	v_mfma_scale_f32_16x16x128_f8f6f4 v[96:99], v[8:15], v[40:47], v[96:99], v216, v216 op_sel_hi:[0,0,0]
	v_mfma_scale_f32_16x16x128_f8f6f4 v[92:95], v[0:7], v[48:55], v[92:95], v216, v216 op_sel_hi:[0,0,0]
	v_mfma_scale_f32_16x16x128_f8f6f4 v[80:83], v[8:15], v[48:55], v[80:83], v216, v216 op_sel_hi:[0,0,0]
	v_mfma_scale_f32_16x16x128_f8f6f4 v[76:79], v[0:7], v[56:63], v[76:79], v216, v216 op_sel_hi:[0,0,0]
	v_mfma_scale_f32_16x16x128_f8f6f4 v[68:71], v[8:15], v[56:63], v[68:71], v216, v216 op_sel_hi:[0,0,0]
	s_setprio 0
	s_setprio 1
	v_mfma_scale_f32_16x16x128_f8f6f4 v[122:125], v[16:23], v[32:39], v[122:125], v216, v216 op_sel_hi:[0,0,0]
	v_mfma_scale_f32_16x16x128_f8f6f4 v[118:121], v[24:31], v[32:39], v[118:121], v216, v216 op_sel_hi:[0,0,0]
	v_mfma_scale_f32_16x16x128_f8f6f4 v[104:107], v[16:23], v[40:47], v[104:107], v216, v216 op_sel_hi:[0,0,0]
	v_mfma_scale_f32_16x16x128_f8f6f4 v[100:103], v[24:31], v[40:47], v[100:103], v216, v216 op_sel_hi:[0,0,0]
	v_mfma_scale_f32_16x16x128_f8f6f4 v[88:91], v[16:23], v[48:55], v[88:91], v216, v216 op_sel_hi:[0,0,0]
	v_mfma_scale_f32_16x16x128_f8f6f4 v[84:87], v[24:31], v[48:55], v[84:87], v216, v216 op_sel_hi:[0,0,0]
	v_mfma_scale_f32_16x16x128_f8f6f4 v[72:75], v[16:23], v[56:63], v[72:75], v216, v216 op_sel_hi:[0,0,0]
	v_mfma_scale_f32_16x16x128_f8f6f4 v[64:67], v[24:31], v[56:63], v[64:67], v216, v216 op_sel_hi:[0,0,0]
	s_setprio 0
	s_barrier
	s_add_i32 s24, s24, 2
	s_add_u32 s22, s22, 0x100
	s_addc_u32 s23, s23, 0
	s_add_u32 s2, s2, 0x100
	s_addc_u32 s3, s3, 0
	s_cmp_gt_u32 s24, 5
	s_cbranch_scc1 .LBB0_505
.LBB0_503:
	ds_read_b128 v[28:31], v230
	ds_read_b128 v[16:19], v231
	ds_read_b128 v[24:27], v226
	ds_read_b128 v[0:3], v227
	ds_read_b128 v[20:23], v232
	ds_read_b128 v[4:7], v233
	ds_read_b128 v[8:11], v234
	ds_read_b128 v[12:15], v235
	s_cmp_eq_u32 s24, 4
	s_cselect_b64 s[4:5], -1, 0
	s_add_i32 m0, s15, 0xc400
	ds_read_b128 v[56:59], v242 offset:1024
	ds_read_b128 v[60:63], v245 offset:1040
	ds_read_b128 v[48:51], v242 offset:3072
	ds_read_b128 v[52:55], v245 offset:3088
	ds_read_b128 v[40:43], v242 offset:5120
	ds_read_b128 v[44:47], v245 offset:5136
	ds_read_b128 v[32:35], v242 offset:7168
	ds_read_b128 v[36:39], v245 offset:7184
	global_load_lds_dwordx4 v200, s[2:3]
	s_add_i32 m0, s15, 0xe400
	s_and_b64 s[6:7], s[56:57], s[4:5]
	global_load_lds_dwordx4 v202, s[2:3]
	s_andn2_b64 vcc, exec, s[6:7]
	s_cbranch_vccz .LBB0_501
	v_mov_b32_e32 v201, v113
	v_mov_b32_e32 v203, v113
	v_mov_b64_e32 v[208:209], v[202:203]
	v_mov_b64_e32 v[210:211], v[200:201]
	s_branch .LBB0_502

.LBB0_1577:
	v_readfirstlane_b32 s24, v5
	s_mul_i32 s7, s7, s24
	s_add_u32 s46, s0, 0x17110100
	s_mul_hi_u32 s7, s24, s7
	s_addc_u32 s47, s1, 0
	s_abs_i32 s23, s8
	s_add_i32 s24, s24, s7
	s_mul_hi_u32 s7, s23, s24
	s_mul_i32 s24, s7, s6
	s_sub_i32 s23, s23, s24
	s_ashr_i32 s22, s8, 31
	s_add_i32 s24, s7, 1
	s_sub_i32 s30, s23, s6
	s_cmp_ge_u32 s23, s6
	s_cselect_b32 s7, s24, s7
	s_cselect_b32 s23, s30, s23
	s_add_i32 s24, s7, 1
	s_cmp_ge_u32 s23, s6
	s_cselect_b32 s6, s24, s7
	s_lshl_b32 s7, s21, 5
	s_xor_b32 s6, s6, s22
	s_and_b32 s65, s7, 0x60
	s_sub_i32 s63, s6, s22
	s_lshl_b32 s64, s20, 6
	s_lshl_b32 s6, s20, 13
	s_lshl_b32 s7, s65, 7
	s_add_i32 s66, s17, 0x18400
	s_add_i32 s67, s17, 0x1a400
	v_lshl_add_u64 v[0:1], v[0:1], 0, s[26:27]
	s_mov_b32 m0, s66
	s_add_u32 s48, s0, 0x63910180
	s_waitcnt vmcnt(2)
	s_barrier
	global_load_lds_dwordx4 v[0:1], off
	v_lshl_add_u64 v[0:1], v[2:3], 0, s[26:27]
	s_mov_b32 m0, s67
	s_addc_u32 s49, s1, 0
	s_add_i32 s68, s17, 0x8400
	s_add_i32 s69, s17, 0xa400
	v_mov_b32_e32 v201, v113
	global_load_lds_dwordx4 v[0:1], off
	v_lshl_add_u64 v[0:1], s[48:49], 0, v[112:113]
	s_mov_b32 m0, s68
	s_add_u32 s0, s2, 0x20080
	global_load_lds_dwordx4 v[0:1], off
	v_lshl_add_u64 v[0:1], s[48:49], 0, v[200:201]
	s_mov_b32 m0, s69
	s_addc_u32 s1, s3, 0
	s_add_i32 s70, s17, 0x1c400
	global_load_lds_dwordx4 v[0:1], off
	v_lshl_add_u64 v[0:1], s[0:1], 0, v[196:197]
	s_mov_b32 m0, s70
	s_add_i32 s71, s17, 0x1e400
	global_load_lds_dwordx4 v[0:1], off
	v_lshl_add_u64 v[0:1], s[0:1], 0, v[194:195]
	s_mov_b32 m0, s71
	v_lshlrev_b32_e32 v2, 6, v4
	global_load_lds_dwordx4 v[0:1], off
	v_lshlrev_b32_e32 v0, 1, v4
	v_lshlrev_b32_e32 v3, 2, v4
	v_and_b32_e32 v0, 32, v0
	v_lshlrev_b32_e32 v1, 5, v4
	v_and_b32_e32 v2, 0x3c0, v2
	v_and_b32_e32 v3, 32, v3
	v_and_b32_e32 v1, 0x400, v1
	v_bitop3_b32 v0, v2, v3, v0 bitop3:0x36
	s_waitcnt vmcnt(6)
	s_and_b32 s73, s5, 0xffffffc0
	s_add_i32 s0, s7, 0
	s_add_i32 s6, s6, 0
	v_add3_u32 v2, s0, v0, v1
	v_add_u32_e32 v0, s6, v0
	s_cmpk_lt_u32 s5, 0x100
	s_sext_i32_i16 s20, s4
	s_mov_b32 s72, 0
	v_add_u32_e32 v224, 0x10400, v2
	v_add_u32_e32 v225, 0x14400, v2
	v_add_u32_e32 v226, 0x18400, v2
	v_add_u32_e32 v227, 0x1c400, v2
	s_cselect_b64 s[50:51], -1, 0
	s_ashr_i32 s74, s64, 31
	v_add_u32_e32 v228, 0x10410, v2
	v_add_u32_e32 v229, 0x10c00, v2
	v_add_u32_e32 v230, 0x10c10, v2
	v_add_u32_e32 v231, 0x14410, v2
	v_add_u32_e32 v232, 0x14c00, v2
	v_add_u32_e32 v233, 0x14c10, v2
	v_add_u32_e32 v234, 0x18410, v2
	v_add_u32_e32 v235, 0x18c00, v2
	v_add_u32_e32 v236, 0x18c10, v2
	v_add_u32_e32 v237, 0x1c410, v2
	v_add_u32_e32 v238, 0x1cc00, v2
	v_add_u32_e32 v239, 0x1cc10, v2
	v_add_u32_e32 v240, v0, v1
	v_mbcnt_lo_u32_b32 v221, -1, 0
	v_mbcnt_hi_u32_b32 v221, -1, v221
	v_and_b32_e32 v221, 16, v221
	v_add_u32_e32 v224, v224, v221
	v_add_u32_e32 v225, v225, v221
	v_add_u32_e32 v226, v226, v221
	v_add_u32_e32 v227, v227, v221
	v_add_u32_e32 v229, v229, v221
	v_add_u32_e32 v232, v232, v221
	v_add_u32_e32 v235, v235, v221
	v_add_u32_e32 v238, v238, v221
	v_sub_u32_e32 v228, v228, v221
	v_sub_u32_e32 v230, v230, v221
	v_sub_u32_e32 v231, v231, v221
	v_sub_u32_e32 v233, v233, v221
	v_sub_u32_e32 v234, v234, v221
	v_sub_u32_e32 v236, v236, v221
	v_sub_u32_e32 v237, v237, v221
	v_sub_u32_e32 v239, v239, v221
	v_sub_u32_e32 v243, v240, v221
	v_add_u32_e32 v240, v240, v221
	s_barrier
	s_branch .LBB0_1580

.LBB0_1586:
	s_waitcnt vmcnt(8)
	s_add_u32 s6, s2, 0x80
	s_waitcnt lgkmcnt(0)
	s_addc_u32 s7, s3, 0
	s_and_b64 s[4:5], s[4:5], exec
	s_cselect_b32 s7, s41, s7
	s_cselect_b32 s6, s40, s6
	s_cselect_b32 s5, s21, s24
	s_cselect_b32 s4, s22, s23
	s_barrier
	s_setprio 1
	s_waitcnt lgkmcnt(0)
	v_mfma_scale_f32_16x16x128_f8f6f4 v[186:189], v[24:31], v[56:63], v[186:189], v216, v216 op_sel_hi:[0,0,0]
	v_mfma_scale_f32_16x16x128_f8f6f4 v[178:181], v[16:23], v[56:63], v[178:181], v216, v216 op_sel_hi:[0,0,0]
	v_mfma_scale_f32_16x16x128_f8f6f4 v[170:173], v[24:31], v[48:55], v[170:173], v216, v216 op_sel_hi:[0,0,0]
	v_mfma_scale_f32_16x16x128_f8f6f4 v[162:165], v[16:23], v[48:55], v[162:165], v216, v216 op_sel_hi:[0,0,0]
	v_mfma_scale_f32_16x16x128_f8f6f4 v[154:157], v[24:31], v[40:47], v[154:157], v216, v216 op_sel_hi:[0,0,0]
	v_mfma_scale_f32_16x16x128_f8f6f4 v[146:149], v[16:23], v[40:47], v[146:149], v216, v216 op_sel_hi:[0,0,0]
	v_mfma_scale_f32_16x16x128_f8f6f4 v[138:141], v[24:31], v[32:39], v[138:141], v216, v216 op_sel_hi:[0,0,0]
	v_mfma_scale_f32_16x16x128_f8f6f4 v[130:133], v[16:23], v[32:39], v[130:133], v216, v216 op_sel_hi:[0,0,0]
	s_setprio 0
	s_setprio 1
	v_mfma_scale_f32_16x16x128_f8f6f4 v[190:193], v[0:7], v[56:63], v[190:193], v216, v216 op_sel_hi:[0,0,0]
	v_mfma_scale_f32_16x16x128_f8f6f4 v[182:185], v[8:15], v[56:63], v[182:185], v216, v216 op_sel_hi:[0,0,0]
	v_mfma_scale_f32_16x16x128_f8f6f4 v[174:177], v[0:7], v[48:55], v[174:177], v216, v216 op_sel_hi:[0,0,0]
	v_mfma_scale_f32_16x16x128_f8f6f4 v[166:169], v[8:15], v[48:55], v[166:169], v216, v216 op_sel_hi:[0,0,0]
	v_mfma_scale_f32_16x16x128_f8f6f4 v[158:161], v[0:7], v[40:47], v[158:161], v216, v216 op_sel_hi:[0,0,0]
	v_mfma_scale_f32_16x16x128_f8f6f4 v[150:153], v[8:15], v[40:47], v[150:153], v216, v216 op_sel_hi:[0,0,0]
	v_mfma_scale_f32_16x16x128_f8f6f4 v[142:145], v[0:7], v[32:39], v[142:145], v216, v216 op_sel_hi:[0,0,0]
	v_mfma_scale_f32_16x16x128_f8f6f4 v[134:137], v[8:15], v[32:39], v[134:137], v216, v216 op_sel_hi:[0,0,0]
	s_setprio 0
	s_barrier
	s_mov_b32 m0, s18
	v_lshl_add_u64 v[244:245], s[4:5], 0, v[196:197]
	s_add_u32 s78, s4, 0x20000
	ds_read_b128 v[32:35], v240 offset:17408
	ds_read_b128 v[36:39], v243 offset:17424
	ds_read_b128 v[40:43], v240 offset:19456
	ds_read_b128 v[44:47], v243 offset:19472
	ds_read_b128 v[48:51], v240 offset:21504
	ds_read_b128 v[52:55], v243 offset:21520
	ds_read_b128 v[56:59], v240 offset:23552
	ds_read_b128 v[60:63], v243 offset:23568
	global_load_lds_dwordx4 v[244:245], off
	v_lshl_add_u64 v[246:247], s[4:5], 0, v[194:195]
	s_mov_b32 m0, s19
	s_addc_u32 s79, s5, 0
	global_load_lds_dwordx4 v[246:247], off
	v_lshl_add_u64 v[248:249], s[78:79], 0, v[196:197]
	s_mov_b32 m0, s28
	v_mov_b32_e32 v201, v113
	global_load_lds_dwordx4 v[248:249], off
	v_lshl_add_u64 v[248:249], s[78:79], 0, v[194:195]
	s_mov_b32 m0, s29
	v_lshl_add_u64 v[250:251], s[6:7], 0, v[200:201]
	global_load_lds_dwordx4 v[248:249], off
	s_mov_b32 m0, s59
	v_lshl_add_u64 v[248:249], s[6:7], 0, v[112:113]
	global_load_lds_dwordx4 v112, s[6:7]
	s_mov_b32 m0, s60
	s_nop 0
	global_load_lds_dwordx4 v200, s[6:7]
	s_waitcnt vmcnt(8)
	s_waitcnt lgkmcnt(0)
	s_barrier
	s_setprio 1
	s_waitcnt lgkmcnt(0)
	v_mfma_scale_f32_16x16x128_f8f6f4 v[122:125], v[24:31], v[32:39], v[122:125], v216, v216 op_sel_hi:[0,0,0]
	v_mfma_scale_f32_16x16x128_f8f6f4 v[114:117], v[16:23], v[32:39], v[114:117], v216, v216 op_sel_hi:[0,0,0]
	v_mfma_scale_f32_16x16x128_f8f6f4 v[104:107], v[24:31], v[40:47], v[104:107], v216, v216 op_sel_hi:[0,0,0]
	v_mfma_scale_f32_16x16x128_f8f6f4 v[96:99], v[16:23], v[40:47], v[96:99], v216, v216 op_sel_hi:[0,0,0]
	v_mfma_scale_f32_16x16x128_f8f6f4 v[88:91], v[24:31], v[48:55], v[88:91], v216, v216 op_sel_hi:[0,0,0]
	v_mfma_scale_f32_16x16x128_f8f6f4 v[80:83], v[16:23], v[48:55], v[80:83], v216, v216 op_sel_hi:[0,0,0]
	v_mfma_scale_f32_16x16x128_f8f6f4 v[72:75], v[24:31], v[56:63], v[72:75], v216, v216 op_sel_hi:[0,0,0]
	v_mfma_scale_f32_16x16x128_f8f6f4 v[68:71], v[16:23], v[56:63], v[68:71], v216, v216 op_sel_hi:[0,0,0]
	s_setprio 0
	s_setprio 1
	v_mfma_scale_f32_16x16x128_f8f6f4 v[126:129], v[0:7], v[32:39], v[126:129], v216, v216 op_sel_hi:[0,0,0]
	v_mfma_scale_f32_16x16x128_f8f6f4 v[118:121], v[8:15], v[32:39], v[118:121], v216, v216 op_sel_hi:[0,0,0]
	v_mfma_scale_f32_16x16x128_f8f6f4 v[108:111], v[0:7], v[40:47], v[108:111], v216, v216 op_sel_hi:[0,0,0]
	v_mfma_scale_f32_16x16x128_f8f6f4 v[100:103], v[8:15], v[40:47], v[100:103], v216, v216 op_sel_hi:[0,0,0]
	v_mfma_scale_f32_16x16x128_f8f6f4 v[92:95], v[0:7], v[48:55], v[92:95], v216, v216 op_sel_hi:[0,0,0]
	v_mfma_scale_f32_16x16x128_f8f6f4 v[84:87], v[8:15], v[48:55], v[84:87], v216, v216 op_sel_hi:[0,0,0]
	v_mfma_scale_f32_16x16x128_f8f6f4 v[76:79], v[0:7], v[56:63], v[76:79], v216, v216 op_sel_hi:[0,0,0]
	v_mfma_scale_f32_16x16x128_f8f6f4 v[64:67], v[8:15], v[56:63], v[64:67], v216, v216 op_sel_hi:[0,0,0]
	s_setprio 0
	s_barrier
	ds_read_b128 v[4:7], v234
	ds_read_b128 v[8:11], v235
	ds_read_b128 v[0:3], v226
	ds_read_b128 v[16:19], v227
	ds_read_b128 v[12:15], v236
	ds_read_b128 v[20:23], v237
	ds_read_b128 v[24:27], v238
	ds_read_b128 v[28:31], v239
	s_mov_b32 m0, s61
	v_lshl_add_u64 v[210:211], s[6:7], 0, v[210:211]
	ds_read_b128 v[32:35], v240 offset:33792
	ds_read_b128 v[36:39], v243 offset:33808
	ds_read_b128 v[40:43], v240 offset:35840
	ds_read_b128 v[44:47], v243 offset:35856
	ds_read_b128 v[48:51], v240 offset:37888
	ds_read_b128 v[52:55], v243 offset:37904
	ds_read_b128 v[56:59], v240 offset:39936
	ds_read_b128 v[60:63], v243 offset:39952
	global_load_lds_dwordx4 v[210:211], off
	v_lshl_add_u64 v[208:209], s[6:7], 0, v[208:209]
	s_mov_b32 m0, s62
	s_nop 0
	global_load_lds_dwordx4 v[208:209], off
	s_waitcnt vmcnt(8)
	s_waitcnt lgkmcnt(0)
	s_barrier
	s_setprio 1
	s_waitcnt lgkmcnt(0)
	v_mfma_scale_f32_16x16x128_f8f6f4 v[186:189], v[0:7], v[32:39], v[186:189], v216, v216 op_sel_hi:[0,0,0]
	v_mfma_scale_f32_16x16x128_f8f6f4 v[178:181], v[8:15], v[32:39], v[178:181], v216, v216 op_sel_hi:[0,0,0]
	v_mfma_scale_f32_16x16x128_f8f6f4 v[170:173], v[0:7], v[40:47], v[170:173], v216, v216 op_sel_hi:[0,0,0]
	v_mfma_scale_f32_16x16x128_f8f6f4 v[162:165], v[8:15], v[40:47], v[162:165], v216, v216 op_sel_hi:[0,0,0]
	v_mfma_scale_f32_16x16x128_f8f6f4 v[154:157], v[0:7], v[48:55], v[154:157], v216, v216 op_sel_hi:[0,0,0]
	v_mfma_scale_f32_16x16x128_f8f6f4 v[146:149], v[8:15], v[48:55], v[146:149], v216, v216 op_sel_hi:[0,0,0]
	v_mfma_scale_f32_16x16x128_f8f6f4 v[138:141], v[0:7], v[56:63], v[138:141], v216, v216 op_sel_hi:[0,0,0]
	v_mfma_scale_f32_16x16x128_f8f6f4 v[130:133], v[8:15], v[56:63], v[130:133], v216, v216 op_sel_hi:[0,0,0]
	s_setprio 0
	s_setprio 1
	v_mfma_scale_f32_16x16x128_f8f6f4 v[190:193], v[16:23], v[32:39], v[190:193], v216, v216 op_sel_hi:[0,0,0]
	v_mfma_scale_f32_16x16x128_f8f6f4 v[182:185], v[24:31], v[32:39], v[182:185], v216, v216 op_sel_hi:[0,0,0]
	v_mfma_scale_f32_16x16x128_f8f6f4 v[174:177], v[16:23], v[40:47], v[174:177], v216, v216 op_sel_hi:[0,0,0]
	v_mfma_scale_f32_16x16x128_f8f6f4 v[166:169], v[24:31], v[40:47], v[166:169], v216, v216 op_sel_hi:[0,0,0]
	v_mfma_scale_f32_16x16x128_f8f6f4 v[158:161], v[16:23], v[48:55], v[158:161], v216, v216 op_sel_hi:[0,0,0]
	v_mfma_scale_f32_16x16x128_f8f6f4 v[150:153], v[24:31], v[48:55], v[150:153], v216, v216 op_sel_hi:[0,0,0]
	v_mfma_scale_f32_16x16x128_f8f6f4 v[142:145], v[16:23], v[56:63], v[142:145], v216, v216 op_sel_hi:[0,0,0]
	v_mfma_scale_f32_16x16x128_f8f6f4 v[134:137], v[24:31], v[56:63], v[134:137], v216, v216 op_sel_hi:[0,0,0]
	s_setprio 0
	s_barrier
	s_mov_b32 m0, s66
	v_lshl_add_u64 v[208:209], v[244:245], 0, s[26:27]
	s_add_u32 s4, s4, 0x20080
	ds_read_b128 v[32:35], v240 offset:50176
	ds_read_b128 v[36:39], v243 offset:50192
	ds_read_b128 v[40:43], v240 offset:52224
	ds_read_b128 v[44:47], v243 offset:52240
	ds_read_b128 v[48:51], v240 offset:54272
	ds_read_b128 v[52:55], v243 offset:54288
	ds_read_b128 v[56:59], v240 offset:56320
	ds_read_b128 v[60:63], v243 offset:56336
	global_load_lds_dwordx4 v[208:209], off
	v_lshl_add_u64 v[208:209], v[246:247], 0, s[26:27]
	s_mov_b32 m0, s67
	s_addc_u32 s5, s5, 0
	global_load_lds_dwordx4 v[208:209], off
	v_lshl_add_u64 v[208:209], s[4:5], 0, v[196:197]
	s_mov_b32 m0, s70
	s_nop 0
	global_load_lds_dwordx4 v[208:209], off
	v_lshl_add_u64 v[208:209], s[4:5], 0, v[194:195]
	s_mov_b32 m0, s71
	s_nop 0
	global_load_lds_dwordx4 v[208:209], off
	v_lshl_add_u64 v[208:209], v[248:249], 0, s[26:27]
	s_mov_b32 m0, s68
	s_nop 0
	global_load_lds_dwordx4 v[208:209], off
	v_lshl_add_u64 v[208:209], v[250:251], 0, s[26:27]
	s_mov_b32 m0, s69
	s_nop 0
	global_load_lds_dwordx4 v[208:209], off
	s_waitcnt vmcnt(8)
	s_waitcnt lgkmcnt(0)
	s_barrier
	s_setprio 1
	s_waitcnt lgkmcnt(0)
	v_mfma_scale_f32_16x16x128_f8f6f4 v[122:125], v[0:7], v[32:39], v[122:125], v216, v216 op_sel_hi:[0,0,0]
	v_mfma_scale_f32_16x16x128_f8f6f4 v[114:117], v[8:15], v[32:39], v[114:117], v216, v216 op_sel_hi:[0,0,0]
	v_mfma_scale_f32_16x16x128_f8f6f4 v[104:107], v[0:7], v[40:47], v[104:107], v216, v216 op_sel_hi:[0,0,0]
	v_mfma_scale_f32_16x16x128_f8f6f4 v[96:99], v[8:15], v[40:47], v[96:99], v216, v216 op_sel_hi:[0,0,0]
	v_mfma_scale_f32_16x16x128_f8f6f4 v[88:91], v[0:7], v[48:55], v[88:91], v216, v216 op_sel_hi:[0,0,0]
	v_mfma_scale_f32_16x16x128_f8f6f4 v[80:83], v[8:15], v[48:55], v[80:83], v216, v216 op_sel_hi:[0,0,0]
	v_mfma_scale_f32_16x16x128_f8f6f4 v[72:75], v[0:7], v[56:63], v[72:75], v216, v216 op_sel_hi:[0,0,0]
	v_mfma_scale_f32_16x16x128_f8f6f4 v[68:71], v[8:15], v[56:63], v[68:71], v216, v216 op_sel_hi:[0,0,0]
	s_setprio 0
	s_setprio 1
	v_mfma_scale_f32_16x16x128_f8f6f4 v[126:129], v[16:23], v[32:39], v[126:129], v216, v216 op_sel_hi:[0,0,0]
	v_mfma_scale_f32_16x16x128_f8f6f4 v[118:121], v[24:31], v[32:39], v[118:121], v216, v216 op_sel_hi:[0,0,0]
	v_mfma_scale_f32_16x16x128_f8f6f4 v[108:111], v[16:23], v[40:47], v[108:111], v216, v216 op_sel_hi:[0,0,0]
	v_mfma_scale_f32_16x16x128_f8f6f4 v[100:103], v[24:31], v[40:47], v[100:103], v216, v216 op_sel_hi:[0,0,0]
	v_mfma_scale_f32_16x16x128_f8f6f4 v[92:95], v[16:23], v[48:55], v[92:95], v216, v216 op_sel_hi:[0,0,0]
	v_mfma_scale_f32_16x16x128_f8f6f4 v[84:87], v[24:31], v[48:55], v[84:87], v216, v216 op_sel_hi:[0,0,0]
	v_mfma_scale_f32_16x16x128_f8f6f4 v[76:79], v[16:23], v[56:63], v[76:79], v216, v216 op_sel_hi:[0,0,0]
	v_mfma_scale_f32_16x16x128_f8f6f4 v[64:67], v[24:31], v[56:63], v[64:67], v216, v216 op_sel_hi:[0,0,0]
	s_setprio 0
	s_barrier
	s_add_i32 s30, s30, 2
	s_add_u32 s23, s23, 0x100
	s_addc_u32 s24, s24, 0
	s_add_u32 s2, s2, 0x100
	s_addc_u32 s3, s3, 0
	s_cmp_gt_u32 s30, 5
	s_cbranch_scc1 .LBB0_1589
.LBB0_1587:
	ds_read_b128 v[28:31], v228
	ds_read_b128 v[16:19], v229
	ds_read_b128 v[24:27], v224
	ds_read_b128 v[0:3], v225
	ds_read_b128 v[20:23], v230
	ds_read_b128 v[4:7], v231
	ds_read_b128 v[8:11], v232
	ds_read_b128 v[12:15], v233
	s_cmp_eq_u32 s30, 4
	s_cselect_b64 s[4:5], -1, 0
	s_add_i32 m0, s17, 0xc400
	ds_read_b128 v[56:59], v240 offset:1024
	ds_read_b128 v[60:63], v243 offset:1040
	ds_read_b128 v[48:51], v240 offset:3072
	ds_read_b128 v[52:55], v243 offset:3088
	ds_read_b128 v[40:43], v240 offset:5120
	ds_read_b128 v[44:47], v243 offset:5136
	ds_read_b128 v[32:35], v240 offset:7168
	ds_read_b128 v[36:39], v243 offset:7184
	global_load_lds_dwordx4 v198, s[2:3]
	s_add_i32 m0, s17, 0xe400
	s_and_b64 s[6:7], s[0:1], s[4:5]
	global_load_lds_dwordx4 v202, s[2:3]
	s_andn2_b64 vcc, exec, s[6:7]
	s_cbranch_vccz .LBB0_1585
	v_mov_b32_e32 v199, v113
	v_mov_b32_e32 v203, v113
	v_mov_b64_e32 v[208:209], v[202:203]
	v_mov_b64_e32 v[210:211], v[198:199]
	s_branch .LBB0_1586
